# loop heads (main loop, topic loop) aligned to 64 bytes
# baseline (speedup 1.0000x reference)
.LBB1_6:
	s_lshr_b32 s57, s46, 2
	s_lshl_b32 s5, s46, 3
	s_lshl_b32 s4, s47, 3
	s_lshr_b32 s60, s47, 2
	s_add_i32 s59, s57, s51
	s_and_b64 s[4:5], s[4:5], s[38:39]
	s_add_i32 s58, s60, s45
	s_lshl_b32 s59, s59, 5
	v_or_b32_e32 v71, s5, v1
	s_lshl_b32 s58, s58, 5
	v_or_b32_e32 v72, s4, v68
	v_or_b32_e32 v71, s59, v71
	v_or_b32_e32 v72, s58, v72
	v_subrev_u32_e32 v74, s52, v71
	v_subrev_u32_e32 v73, s50, v72
	v_cmp_gt_i32_e32 vcc, s54, v74
	v_add_u32_e32 v75, 0xc8, v74
	v_add_u32_e32 v76, 0xc8, v73
	v_cndmask_b32_e64 v74, 0, 1, vcc
	v_cmp_gt_i32_e32 vcc, s49, v73
	v_cmp_gt_i32_e64 s[4:5], s53, v75
	s_cmp_lt_u32 s57, s55
	v_cndmask_b32_e64 v73, 0, 1, vcc
	v_cmp_gt_i32_e32 vcc, s48, v76
	s_cselect_b64 s[58:59], -1, 0
	s_cmp_lt_u32 s60, s42
	v_cndmask_b32_e64 v76, 0, 1, vcc
	v_cmp_gt_i32_e32 vcc, s50, v72
	v_cndmask_b32_e64 v72, 0, 1, s[4:5]
	v_cmp_gt_i32_e64 s[4:5], s52, v71
	s_cselect_b64 s[60:61], -1, 0
	s_lshl_b32 s62, 1, s46
	v_cndmask_b32_e64 v71, v74, v72, s[4:5]
	v_cndmask_b32_e32 v72, v73, v76, vcc
	v_and_b32_e32 v71, 1, v71
	v_and_b32_e32 v72, 1, v72
	v_cmp_eq_u32_e32 vcc, 1, v71
	s_lshl_b32 s57, 1, s47
	v_mov_b32_e32 v75, s62
	v_cmp_eq_u32_e64 s[4:5], 1, v72
	s_and_b64 vcc, s[58:59], vcc
	v_mov_b32_e32 v77, s57
	v_cndmask_b32_e32 v71, 0, v75, vcc
	s_and_b64 vcc, s[60:61], s[4:5]
	s_add_i32 s47, s47, 2
	s_add_i32 s46, s46, 2
	s_add_i32 s56, s56, -2
	v_cndmask_b32_e32 v72, 0, v77, vcc
	v_or_b32_e32 v70, v71, v70
	s_cmp_lg_u32 s56, 0
	v_or_b32_e32 v69, v72, v69
	s_cbranch_scc1 .LBB1_6
	v_lshrrev_b32_e32 v1, 1, v212
	v_xor_b32_e32 v72, v1, v68
	v_and_b32_e32 v196, 1, v0
	v_bitop3_b32 v1, v1, v68, 8 bitop3:0x1e
	v_lshlrev_b32_e32 v71, 9, v68
	v_lshlrev_b32_e32 v73, 3, v196
	v_lshlrev_b32_e32 v1, 4, v1
	v_or3_b32 v201, v1, v71, v73
	v_lshrrev_b32_e32 v1, 5, v212
	v_lshlrev_b32_e32 v72, 4, v72
	v_and_b32_e32 v68, 0x100, v0
	v_bitop3_b32 v74, v1, v0, 15 bitop3:0x78
	v_and_b32_e32 v214, 31, v0
	v_lshl_or_b32 v204, v214, 9, v68
	v_lshlrev_b32_e32 v203, 4, v74
	v_or3_b32 v202, v72, v71, v73
	v_or_b32_e32 v205, v69, v70
	s_waitcnt vmcnt(23)
	v_cvt_pk_f16_f32 v68, v62, v63
	v_cvt_pk_f16_f32 v69, v64, v65
	ds_write_b64 v202, v[68:69]
	v_and_b32_e32 v68, 1, v205
	v_cmp_eq_u32_e32 vcc, 0, v68
	s_mov_b32 s39, 0
	s_movk_i32 s45, 0x2000
	v_cndmask_b32_e64 v68, 1.0, 0, vcc
	v_pk_fma_f32 v[62:63], v[68:69], v[62:63], 0 op_sel_hi:[0,1,0]
	v_pk_fma_f32 v[64:65], v[68:69], v[64:65], 0 op_sel_hi:[0,1,0]
	s_waitcnt vmcnt(21)
	v_cvt_pk_f16_f32 v68, v58, v59
	v_cvt_pk_f16_f32 v69, v60, v61
	ds_write_b64 v201, v[68:69] offset:4096
	v_and_b32_e32 v68, 2, v205
	v_cmp_eq_u32_e32 vcc, 0, v68
	s_nop 1
	v_cndmask_b32_e64 v68, 1.0, 0, vcc
	v_pk_fma_f32 v[58:59], v[68:69], v[58:59], v[62:63] op_sel_hi:[0,1,1]
	s_waitcnt vmcnt(19)
	v_cvt_pk_f16_f32 v62, v54, v55
	v_cvt_pk_f16_f32 v63, v56, v57
	ds_write_b64 v202, v[62:63] offset:8192
	v_and_b32_e32 v62, 4, v205
	v_cmp_eq_u32_e32 vcc, 0, v62
	v_pk_fma_f32 v[60:61], v[68:69], v[60:61], v[64:65] op_sel_hi:[0,1,1]
	s_nop 0
	v_cndmask_b32_e64 v62, 1.0, 0, vcc
	v_pk_fma_f32 v[54:55], v[62:63], v[54:55], v[58:59] op_sel_hi:[0,1,1]
	s_waitcnt vmcnt(17)
	v_cvt_pk_f16_f32 v58, v50, v51
	v_cvt_pk_f16_f32 v59, v52, v53
	ds_write_b64 v201, v[58:59] offset:12288
	v_and_b32_e32 v58, 8, v205
	v_cmp_eq_u32_e32 vcc, 0, v58
	v_pk_fma_f32 v[56:57], v[62:63], v[56:57], v[60:61] op_sel_hi:[0,1,1]
	s_nop 0
	v_cndmask_b32_e64 v58, 1.0, 0, vcc
	v_pk_fma_f32 v[50:51], v[58:59], v[50:51], v[54:55] op_sel_hi:[0,1,1]
	v_pk_fma_f32 v[52:53], v[58:59], v[52:53], v[56:57] op_sel_hi:[0,1,1]
	v_cvt_pk_f16_f32 v50, v50, v51
	v_cvt_pk_f16_f32 v51, v52, v53
	v_or_b32_e32 v52, 0x20000, v202
	ds_write_b64 v52, v[50:51]
	v_cvt_pk_f16_f32 v50, v46, v47
	v_cvt_pk_f16_f32 v51, v48, v49
	ds_write_b64 v202, v[50:51] offset:16384
	v_and_b32_e32 v50, 16, v205
	v_cmp_eq_u32_e32 vcc, 0, v50
	s_nop 1
	v_cndmask_b32_e64 v50, 1.0, 0, vcc
	v_pk_fma_f32 v[46:47], v[50:51], v[46:47], 0 op_sel_hi:[0,1,0]
	v_pk_fma_f32 v[48:49], v[50:51], v[48:49], 0 op_sel_hi:[0,1,0]
	v_cvt_pk_f16_f32 v50, v42, v43
	v_cvt_pk_f16_f32 v51, v44, v45
	ds_write_b64 v201, v[50:51] offset:20480
	v_and_b32_e32 v50, 32, v205
	v_cmp_eq_u32_e32 vcc, 0, v50
	s_nop 1
	v_cndmask_b32_e64 v50, 1.0, 0, vcc
	v_pk_fma_f32 v[42:43], v[50:51], v[42:43], v[46:47] op_sel_hi:[0,1,1]
	v_cvt_pk_f16_f32 v46, v38, v39
	v_cvt_pk_f16_f32 v47, v40, v41
	ds_write_b64 v202, v[46:47] offset:24576
	v_and_b32_e32 v46, 64, v205
	v_cmp_eq_u32_e32 vcc, 0, v46
	v_pk_fma_f32 v[44:45], v[50:51], v[44:45], v[48:49] op_sel_hi:[0,1,1]
	s_nop 0
	v_cndmask_b32_e64 v46, 1.0, 0, vcc
	v_pk_fma_f32 v[38:39], v[46:47], v[38:39], v[42:43] op_sel_hi:[0,1,1]
	s_waitcnt vmcnt(16)
	v_cvt_pk_f16_f32 v42, v34, v35
	v_cvt_pk_f16_f32 v43, v36, v37
	ds_write_b64 v201, v[42:43] offset:28672
	v_and_b32_e32 v42, 0x80, v205
	v_cmp_eq_u32_e32 vcc, 0, v42
	v_pk_fma_f32 v[40:41], v[46:47], v[40:41], v[44:45] op_sel_hi:[0,1,1]
	s_nop 0
	v_cndmask_b32_e64 v42, 1.0, 0, vcc
	v_pk_fma_f32 v[34:35], v[42:43], v[34:35], v[38:39] op_sel_hi:[0,1,1]
	v_pk_fma_f32 v[36:37], v[42:43], v[36:37], v[40:41] op_sel_hi:[0,1,1]
	v_cvt_pk_f16_f32 v34, v34, v35
	v_cvt_pk_f16_f32 v35, v36, v37
	v_or_b32_e32 v36, 0x21000, v201
	ds_write_b64 v36, v[34:35]
	s_waitcnt vmcnt(15)
	v_cvt_pk_f16_f32 v34, v30, v31
	v_cvt_pk_f16_f32 v35, v32, v33
	ds_write_b64 v202, v[34:35] offset:32768
	v_and_b32_e32 v34, 0x100, v205
	v_cmp_eq_u32_e32 vcc, 0, v34
	s_waitcnt vmcnt(13)
	v_cvt_pk_f16_f32 v34, v26, v27
	v_cvt_pk_f16_f32 v35, v28, v29
	ds_write_b64 v201, v[34:35] offset:36864
	v_and_b32_e32 v34, 0x200, v205
	v_cndmask_b32_e64 v186, 1.0, 0, vcc
	v_cmp_eq_u32_e32 vcc, 0, v34
	v_mov_b32_e32 v187, v186
	v_pk_fma_f32 v[30:31], v[186:187], v[30:31], 0 op_sel_hi:[0,1,0]
	v_cndmask_b32_e64 v188, 1.0, 0, vcc
	v_mov_b32_e32 v189, v188
	v_pk_fma_f32 v[26:27], v[188:189], v[26:27], v[30:31] op_sel_hi:[0,1,1]
	s_waitcnt vmcnt(11)
	v_cvt_pk_f16_f32 v30, v22, v23
	v_cvt_pk_f16_f32 v31, v24, v25
	ds_write_b64 v202, v[30:31] offset:40960
	v_and_b32_e32 v30, 0x400, v205
	v_cmp_eq_u32_e32 vcc, 0, v30
	v_pk_fma_f32 v[32:33], v[186:187], v[32:33], 0 op_sel_hi:[0,1,0]
	v_pk_fma_f32 v[28:29], v[188:189], v[28:29], v[32:33] op_sel_hi:[0,1,1]
	v_cndmask_b32_e64 v190, 1.0, 0, vcc
	v_mov_b32_e32 v191, v190
	v_pk_fma_f32 v[22:23], v[190:191], v[22:23], v[26:27] op_sel_hi:[0,1,1]
	s_waitcnt vmcnt(9)
	v_cvt_pk_f16_f32 v26, v18, v19
	v_cvt_pk_f16_f32 v27, v20, v21
	ds_write_b64 v201, v[26:27] offset:45056
	v_and_b32_e32 v26, 0x800, v205
	v_cmp_eq_u32_e32 vcc, 0, v26
	v_pk_fma_f32 v[24:25], v[190:191], v[24:25], v[28:29] op_sel_hi:[0,1,1]
	s_nop 0
	v_cndmask_b32_e64 v192, 1.0, 0, vcc
	v_mov_b32_e32 v193, v192
	v_pk_fma_f32 v[18:19], v[192:193], v[18:19], v[22:23] op_sel_hi:[0,1,1]
	v_pk_fma_f32 v[20:21], v[192:193], v[20:21], v[24:25] op_sel_hi:[0,1,1]
	v_cvt_pk_f16_f32 v18, v18, v19
	v_cvt_pk_f16_f32 v19, v20, v21
	v_or_b32_e32 v20, 0x22000, v202
	ds_write_b64 v20, v[18:19]
	v_cvt_pk_f16_f32 v18, v14, v15
	v_cvt_pk_f16_f32 v19, v16, v17
	ds_write_b64 v202, v[18:19] offset:49152
	v_and_b32_e32 v18, 0x1000, v205
	v_cmp_eq_u32_e32 vcc, 0, v18
	v_cvt_pk_f16_f32 v18, v10, v11
	v_cvt_pk_f16_f32 v19, v12, v13
	ds_write_b64 v201, v[18:19] offset:53248
	v_and_b32_e32 v18, 0x2000, v205
	v_cndmask_b32_e64 v178, 1.0, 0, vcc
	v_cmp_eq_u32_e32 vcc, 0, v18
	v_mov_b32_e32 v179, v178
	v_pk_fma_f32 v[14:15], v[178:179], v[14:15], 0 op_sel_hi:[0,1,0]
	v_cndmask_b32_e64 v180, 1.0, 0, vcc
	v_mov_b32_e32 v181, v180
	v_pk_fma_f32 v[10:11], v[180:181], v[10:11], v[14:15] op_sel_hi:[0,1,1]
	v_cvt_pk_f16_f32 v14, v6, v7
	v_cvt_pk_f16_f32 v15, v8, v9
	ds_write_b64 v202, v[14:15] offset:57344
	v_and_b32_e32 v14, 0x4000, v205
	v_cmp_eq_u32_e32 vcc, 0, v14
	v_pk_fma_f32 v[16:17], v[178:179], v[16:17], 0 op_sel_hi:[0,1,0]
	v_pk_fma_f32 v[12:13], v[180:181], v[12:13], v[16:17] op_sel_hi:[0,1,1]
	v_cndmask_b32_e64 v182, 1.0, 0, vcc
	v_mov_b32_e32 v183, v182
	v_pk_fma_f32 v[6:7], v[182:183], v[6:7], v[10:11] op_sel_hi:[0,1,1]
	s_waitcnt vmcnt(8)
	v_cvt_pk_f16_f32 v10, v2, v3
	v_cvt_pk_f16_f32 v11, v4, v5
	ds_write_b64 v201, v[10:11] offset:61440
	v_and_b32_e32 v10, 0x8000, v205
	v_cmp_eq_u32_e32 vcc, 0, v10
	v_pk_fma_f32 v[8:9], v[182:183], v[8:9], v[12:13] op_sel_hi:[0,1,1]
	s_nop 0
	v_cndmask_b32_e64 v184, 1.0, 0, vcc
	v_mov_b32_e32 v185, v184
	v_pk_fma_f32 v[2:3], v[184:185], v[2:3], v[6:7] op_sel_hi:[0,1,1]
	v_pk_fma_f32 v[4:5], v[184:185], v[4:5], v[8:9] op_sel_hi:[0,1,1]
	v_cvt_pk_f16_f32 v2, v2, v3
	v_cvt_pk_f16_f32 v3, v4, v5
	v_or_b32_e32 v4, 0x23000, v201
	ds_write_b64 v4, v[2:3]
	v_mov_b32_e32 v2, 0
	s_add_i32 s46, s42, -1
	v_lshl_add_u64 v[194:195], s[40:41], 0, v[66:67]
	v_or_b32_e32 v206, 0x20000, v204
	s_mov_b32 s41, -3
	s_movk_i32 s40, 0x3000
	s_mov_b32 s4, s20
	s_mov_b32 s5, s21
	s_mov_b32 s20, 0
	v_mov_b32_e32 v3, v2
	v_mov_b32_e32 v4, v2
	v_mov_b32_e32 v5, v2
	v_mov_b32_e32 v6, v2
	v_mov_b32_e32 v7, v2
	v_mov_b32_e32 v8, v2
	v_mov_b32_e32 v9, v2
	v_mov_b32_e32 v10, v2
	v_mov_b32_e32 v11, v2
	v_mov_b32_e32 v12, v2
	v_mov_b32_e32 v13, v2
	v_mov_b32_e32 v14, v2
	v_mov_b32_e32 v15, v2
	v_mov_b32_e32 v16, v2
	v_mov_b32_e32 v17, v2
	v_mov_b32_e32 v34, v2
	v_mov_b32_e32 v35, v2
	v_mov_b32_e32 v36, v2
	v_mov_b32_e32 v37, v2
	v_mov_b32_e32 v38, v2
	v_mov_b32_e32 v39, v2
	v_mov_b32_e32 v40, v2
	v_mov_b32_e32 v41, v2
	v_mov_b32_e32 v42, v2
	v_mov_b32_e32 v43, v2
	v_mov_b32_e32 v44, v2
	v_mov_b32_e32 v45, v2
	v_mov_b32_e32 v46, v2
	v_mov_b32_e32 v47, v2
	v_mov_b32_e32 v48, v2
	v_mov_b32_e32 v49, v2
	v_mov_b32_e32 v50, v2
	v_mov_b32_e32 v51, v2
	v_mov_b32_e32 v52, v2
	v_mov_b32_e32 v53, v2
	v_mov_b32_e32 v54, v2
	v_mov_b32_e32 v55, v2
	v_mov_b32_e32 v56, v2
	v_mov_b32_e32 v57, v2
	v_mov_b32_e32 v58, v2
	v_mov_b32_e32 v59, v2
	v_mov_b32_e32 v60, v2
	v_mov_b32_e32 v61, v2
	v_mov_b32_e32 v62, v2
	v_mov_b32_e32 v63, v2
	v_mov_b32_e32 v64, v2
	v_mov_b32_e32 v65, v2
	v_mov_b32_e32 v18, v2
	v_mov_b32_e32 v19, v2
	v_mov_b32_e32 v20, v2
	v_mov_b32_e32 v21, v2
	v_mov_b32_e32 v22, v2
	v_mov_b32_e32 v23, v2
	v_mov_b32_e32 v24, v2
	v_mov_b32_e32 v25, v2
	v_mov_b32_e32 v26, v2
	v_mov_b32_e32 v27, v2
	v_mov_b32_e32 v28, v2
	v_mov_b32_e32 v29, v2
	v_mov_b32_e32 v30, v2
	v_mov_b32_e32 v31, v2
	v_mov_b32_e32 v32, v2
	v_mov_b32_e32 v33, v2
	v_mov_b32_e32 v66, v2
	v_mov_b32_e32 v67, v2
	v_mov_b32_e32 v68, v2
	v_mov_b32_e32 v69, v2
	v_mov_b32_e32 v70, v2
	v_mov_b32_e32 v71, v2
	v_mov_b32_e32 v72, v2
	v_mov_b32_e32 v73, v2
	v_mov_b32_e32 v74, v2
	v_mov_b32_e32 v75, v2
	v_mov_b32_e32 v76, v2
	v_mov_b32_e32 v77, v2
	v_mov_b32_e32 v78, v2
	v_mov_b32_e32 v79, v2
	v_mov_b32_e32 v80, v2
	v_mov_b32_e32 v81, v2
	s_add_i32 s75, s44, 1
	s_lshl_b32 s75, s75, 10
	s_and_b32 s75, s75, 0x1c00
	s_min_u32 s76, 2, s46
	s_lshl_b32 s76, s76, 18
	s_or_b32 s75, s75, s76
	s_mov_b32 s76, 0
	v_add_u32_e32 v154, s76, v197
	v_add_u32_e32 v155, s76, v198
	v_add_u32_e32 v156, s76, v199
	v_add_u32_e32 v157, s76, v200
	buffer_load_dwordx4 v[174:177], v154, s[4:7], s75 offen sc0 nt sc1
	buffer_load_dwordx4 v[170:173], v155, s[4:7], s75 offen sc0 nt sc1
	buffer_load_dwordx4 v[162:165], v156, s[4:7], s75 offen sc0 nt sc1
	buffer_load_dwordx4 v[154:157], v157, s[4:7], s75 offen sc0 nt sc1
	s_waitcnt lgkmcnt(0)
	s_barrier
	.p2align	6

.LBB1_53:
	s_or_b64 exec, exec, s[2:3]
	v_add_f32_e32 v130, v130, v14
	v_or_b32_e32 v14, v212, v214
	v_add_f32_e32 v134, v134, v10
	v_add_f32_e32 v10, v110, v50
	v_add_f32_e32 v50, v98, v58
	v_add_f32_e32 v58, v90, v62
	v_add_u32_e32 v62, 0x17080, v14
	v_add_f32_e32 v131, v131, v15
	v_add_f32_e32 v132, v132, v16
	v_add_f32_e32 v133, v133, v17
	v_add_f32_e32 v82, v82, v30
	ds_read_b128 v[14:17], v62
	v_add_f32_e32 v83, v83, v31
	v_add_f32_e32 v84, v84, v32
	v_add_f32_e32 v85, v85, v33
	ds_read_b128 v[30:33], v62 offset:32
	v_add_f32_e32 v2, v142, v2
	v_add_f32_e32 v138, v138, v6
	v_add_f32_e32 v6, v126, v34
	v_add_f32_e32 v34, v122, v38
	v_add_f32_e32 v38, v118, v42
	v_add_f32_e32 v114, v114, v46
	v_add_f32_e32 v42, v106, v54
	v_add_f32_e32 v18, v102, v18
	v_add_f32_e32 v46, v94, v22
	v_add_f32_e32 v141, v141, v9
	v_add_f32_e32 v135, v135, v11
	v_add_f32_e32 v136, v136, v12
	v_add_f32_e32 v137, v137, v13
	v_add_f32_e32 v9, v129, v37
	v_add_f32_e32 v37, v125, v41
	v_add_f32_e32 v41, v121, v45
	v_add_f32_e32 v115, v115, v47
	v_add_f32_e32 v116, v116, v48
	v_add_f32_e32 v117, v117, v49
	v_add_f32_e32 v11, v111, v51
	v_add_f32_e32 v12, v112, v52
	v_add_f32_e32 v13, v113, v53
	v_add_f32_e32 v45, v109, v57
	v_add_f32_e32 v51, v99, v59
	v_add_f32_e32 v52, v100, v60
	v_add_f32_e32 v53, v101, v61
	v_add_f32_e32 v59, v91, v63
	v_add_f32_e32 v60, v92, v64
	v_add_f32_e32 v61, v93, v65
	v_add_f32_e32 v57, v86, v26
	s_waitcnt lgkmcnt(1)
	v_add_f32_e32 v2, v14, v2
	v_add_f32_e32 v6, v14, v6
	v_add_f32_e32 v10, v14, v10
	v_add_f32_e32 v14, v14, v18
	s_waitcnt lgkmcnt(0)
	v_add_f32_e32 v18, v30, v138
	v_add_f32_e32 v22, v30, v34
	v_add_f32_e32 v26, v30, v42
	v_add_f32_e32 v30, v30, v46
	ds_read_b128 v[46:49], v62 offset:64
	ds_read_b128 v[62:65], v62 offset:96
	v_add_f32_e32 v3, v143, v3
	v_add_f32_e32 v4, v144, v4
	v_add_f32_e32 v5, v145, v5
	v_add_f32_e32 v139, v139, v7
	v_add_f32_e32 v140, v140, v8
	v_add_f32_e32 v7, v127, v35
	v_add_f32_e32 v8, v128, v36
	v_add_f32_e32 v35, v123, v39
	v_add_f32_e32 v36, v124, v40
	v_add_f32_e32 v39, v119, v43
	v_add_f32_e32 v40, v120, v44
	v_add_f32_e32 v43, v107, v55
	v_add_f32_e32 v44, v108, v56
	v_add_f32_e32 v19, v103, v19
	v_add_f32_e32 v20, v104, v20
	v_add_f32_e32 v21, v105, v21
	v_add_f32_e32 v54, v95, v23
	v_add_f32_e32 v55, v96, v24
	v_add_f32_e32 v56, v97, v25
	v_add_f32_e32 v86, v87, v27
	v_add_f32_e32 v87, v88, v28
	v_add_f32_e32 v88, v89, v29
	v_add_f32_e32 v3, v15, v3
	v_add_f32_e32 v4, v16, v4
	v_add_f32_e32 v5, v17, v5
	v_add_f32_e32 v7, v15, v7
	v_add_f32_e32 v8, v16, v8
	v_add_f32_e32 v9, v17, v9
	v_add_f32_e32 v11, v15, v11
	v_add_f32_e32 v12, v16, v12
	v_add_f32_e32 v13, v17, v13
	v_add_f32_e32 v15, v15, v19
	v_add_f32_e32 v16, v16, v20
	v_add_f32_e32 v17, v17, v21
	v_add_f32_e32 v19, v31, v139
	v_add_f32_e32 v20, v32, v140
	v_add_f32_e32 v21, v33, v141
	v_add_f32_e32 v23, v31, v35
	v_add_f32_e32 v24, v32, v36
	v_add_f32_e32 v25, v33, v37
	v_add_f32_e32 v27, v31, v43
	v_add_f32_e32 v28, v32, v44
	v_add_f32_e32 v29, v33, v45
	v_add_f32_e32 v31, v31, v54
	v_add_f32_e32 v32, v32, v55
	v_add_f32_e32 v33, v33, v56
	s_waitcnt lgkmcnt(1)
	v_add_f32_e32 v34, v46, v134
	v_add_f32_e32 v38, v46, v38
	v_add_f32_e32 v42, v46, v50
	v_add_f32_e32 v43, v47, v51
	v_add_f32_e32 v44, v48, v52
	v_add_f32_e32 v45, v49, v53
	v_add_f32_e32 v46, v46, v57
	s_waitcnt lgkmcnt(0)
	v_add_f32_e32 v50, v62, v130
	v_add_f32_e32 v51, v63, v131
	v_add_f32_e32 v52, v64, v132
	v_add_f32_e32 v53, v65, v133
	v_add_f32_e32 v54, v62, v114
	v_add_f32_e32 v55, v63, v115
	v_add_f32_e32 v56, v64, v116
	v_add_f32_e32 v57, v65, v117
	v_add_f32_e32 v58, v62, v58
	v_add_f32_e32 v59, v63, v59
	v_add_f32_e32 v60, v64, v60
	v_add_f32_e32 v61, v65, v61
	v_add_f32_e32 v62, v62, v82
	v_add_f32_e32 v63, v63, v83
	v_add_f32_e32 v64, v64, v84
	v_add_f32_e32 v65, v65, v85
	s_waitcnt vmcnt(3)
	v_fma_f32 v82, v66, v2, 0
	v_fma_f32 v83, v66, v6, 0
	v_fma_f32 v84, v66, v10, 0
	v_fma_f32 v85, v66, v14, 0
	v_fmac_f32_e32 v82, v67, v3
	v_fmac_f32_e32 v83, v67, v7
	v_fmac_f32_e32 v84, v67, v11
	v_fmac_f32_e32 v85, v67, v15
	v_fmac_f32_e32 v82, v68, v4
	v_fmac_f32_e32 v83, v68, v8
	v_fmac_f32_e32 v84, v68, v12
	v_fmac_f32_e32 v85, v68, v16
	v_fmac_f32_e32 v82, v69, v5
	v_fmac_f32_e32 v83, v69, v9
	v_fmac_f32_e32 v84, v69, v13
	v_fmac_f32_e32 v85, v69, v17
	s_waitcnt vmcnt(2)
	v_fmac_f32_e32 v82, v70, v18
	v_fmac_f32_e32 v83, v70, v22
	v_fmac_f32_e32 v84, v70, v26
	v_fmac_f32_e32 v85, v70, v30
	v_fmac_f32_e32 v82, v71, v19
	v_fmac_f32_e32 v83, v71, v23
	v_fmac_f32_e32 v84, v71, v27
	v_fmac_f32_e32 v85, v71, v31
	v_fmac_f32_e32 v82, v72, v20
	v_fmac_f32_e32 v83, v72, v24
	v_fmac_f32_e32 v84, v72, v28
	v_fmac_f32_e32 v85, v72, v32
	v_fmac_f32_e32 v82, v73, v21
	v_fmac_f32_e32 v83, v73, v25
	v_fmac_f32_e32 v84, v73, v29
	v_fmac_f32_e32 v85, v73, v33
	v_add_f32_e32 v35, v47, v135
	v_add_f32_e32 v39, v47, v39
	v_add_f32_e32 v47, v47, v86
	s_waitcnt vmcnt(1)
	v_fmac_f32_e32 v82, v74, v34
	v_fmac_f32_e32 v83, v74, v38
	v_fmac_f32_e32 v84, v74, v42
	v_fmac_f32_e32 v85, v74, v46
	v_add_f32_e32 v36, v48, v136
	v_add_f32_e32 v40, v48, v40
	v_add_f32_e32 v48, v48, v87
	v_fmac_f32_e32 v82, v75, v35
	v_fmac_f32_e32 v83, v75, v39
	v_fmac_f32_e32 v84, v75, v43
	v_fmac_f32_e32 v85, v75, v47
	v_add_f32_e32 v37, v49, v137
	v_add_f32_e32 v41, v49, v41
	v_add_f32_e32 v49, v49, v88
	v_fmac_f32_e32 v82, v76, v36
	v_fmac_f32_e32 v83, v76, v40
	v_fmac_f32_e32 v84, v76, v44
	v_fmac_f32_e32 v85, v76, v48
	v_fmac_f32_e32 v82, v77, v37
	v_fmac_f32_e32 v83, v77, v41
	v_fmac_f32_e32 v84, v77, v45
	v_fmac_f32_e32 v85, v77, v49
	s_waitcnt vmcnt(0)
	v_fmac_f32_e32 v82, v78, v50
	v_fmac_f32_e32 v83, v78, v54
	v_fmac_f32_e32 v84, v78, v58
	v_fmac_f32_e32 v85, v78, v62
	v_mul_u32_u24_e32 v87, 10, v225
	v_lshlrev_b32_e32 v1, 9, v1
	v_fmac_f32_e32 v82, v79, v51
	v_fmac_f32_e32 v83, v79, v55
	v_fmac_f32_e32 v84, v79, v59
	v_fmac_f32_e32 v85, v79, v63
	v_lshlrev_b32_e32 v86, 9, v87
	v_lshl_or_b32 v1, v87, 12, v1
	v_lshlrev_b32_e32 v87, 10, v224
	v_fmac_f32_e32 v82, v80, v52
	v_fmac_f32_e32 v83, v80, v56
	v_fmac_f32_e32 v84, v80, v60
	v_fmac_f32_e32 v85, v80, v64
	v_or3_b32 v1, v87, v1, v211
	v_fmac_f32_e32 v82, v81, v53
	v_fmac_f32_e32 v83, v81, v57
	v_fmac_f32_e32 v84, v81, v61
	v_fmac_f32_e32 v85, v81, v65
	v_or3_b32 v86, v86, v212, v214
	v_add_u32_e32 v1, 0x2800, v1
	s_mov_b32 s0, 0
	v_mul_f32_e32 v66, 0.5, v66
	v_mul_f32_e32 v67, 0.5, v67
	v_mul_f32_e32 v68, 0.5, v68
	v_mul_f32_e32 v69, 0.5, v69
	v_mul_f32_e32 v70, 0.5, v70
	v_mul_f32_e32 v71, 0.5, v71
	v_mul_f32_e32 v72, 0.5, v72
	v_mul_f32_e32 v73, 0.5, v73
	v_mul_f32_e32 v74, 0.5, v74
	v_mul_f32_e32 v75, 0.5, v75
	v_mul_f32_e32 v76, 0.5, v76
	v_mul_f32_e32 v77, 0.5, v77
	v_mul_f32_e32 v78, 0.5, v78
	v_mul_f32_e32 v79, 0.5, v79
	v_mul_f32_e32 v80, 0.5, v80
	v_mul_f32_e32 v81, 0.5, v81
	v_mul_f32_e32 v82, 0.5, v82
	v_mul_f32_e32 v83, 0.5, v83
	v_mul_f32_e32 v84, 0.5, v84
	v_mul_f32_e32 v85, 0.5, v85
	v_add_u32_e32 v152, s0, v86
	ds_read_b128 v[88:91], v152
	ds_read_b128 v[92:95], v152 offset:32
	ds_read_b128 v[96:99], v152 offset:64
	ds_read_b128 v[100:103], v152 offset:96
	s_addk_i32 s0, 0x200
	.p2align	6
